# baseline (speedup 1.0000x reference)
.LBB4_39:
	s_or_b64 exec, exec, s[32:33]
	ds_read_b128 v[26:29], v86
	ds_read_b128 v[30:33], v86 offset:1024
	ds_read_b128 v[106:109], v86 offset:2048
	ds_read_b128 v[110:113], v86 offset:3072
	s_waitcnt lgkmcnt(2)
	v_mfma_f32_16x16x32_f16 v[34:37], v[26:29], v[40:43], 0
	v_mfma_f32_16x16x32_f16 v[114:117], v[26:29], v[48:51], 0
	v_mfma_f32_16x16x32_f16 v[118:121], v[26:29], v[56:59], 0
	v_mfma_f32_16x16x32_f16 v[34:37], v[30:33], v[44:47], v[34:37]
	v_mfma_f32_16x16x32_f16 v[114:117], v[30:33], v[52:55], v[114:117]
	v_mfma_f32_16x16x32_f16 v[118:121], v[30:33], v[60:63], v[118:121]
	s_waitcnt lgkmcnt(0)
	v_mfma_f32_16x16x32_f16 v[122:125], v[106:109], v[40:43], 0
	v_mfma_f32_16x16x32_f16 v[122:125], v[110:113], v[44:47], v[122:125]
	s_add_u32 s16, s20, s0
	s_addc_u32 s17, s21, s1
	s_load_dwordx8 s[36:43], s[16:17], 0x16900
	s_load_dwordx8 s[44:51], s[16:17], 0x16920
	s_load_dwordx8 s[52:59], s[16:17], 0x16940
	s_load_dwordx8 s[60:67], s[16:17], 0x16960
	s_load_dwordx4 s[68:71], s[16:17], 0x16980
	s_load_dwordx8 s[72:79], s[16:17], 0x16b40
	s_load_dwordx8 s[80:87], s[16:17], 0x16b60
	s_load_dwordx8 s[88:95], s[16:17], 0x16b80
	s_load_dwordx4 s[96:99], s[16:17], 0x16ba0
	s_load_dwordx8 s[8:15], s[16:17], 0x16bb0
	s_nop 2
	v_cvt_pk_f16_f32 v34, v34, v35
	v_cvt_pk_f16_f32 v35, v36, v37
	ds_write_b64 v88, v[34:35]
	v_cvt_pk_f16_f32 v114, v114, v115
	v_cvt_pk_f16_f32 v115, v116, v117
	ds_write_b64 v90, v[114:115]
	v_cvt_pk_f16_f32 v118, v118, v119
	v_cvt_pk_f16_f32 v119, v120, v121
	ds_write_b64 v92, v[118:119]
	v_mfma_f32_16x16x32_f16 v[34:37], v[106:109], v[48:51], 0
	v_mfma_f32_16x16x32_f16 v[114:117], v[106:109], v[56:59], 0
	v_mfma_f32_16x16x32_f16 v[34:37], v[110:113], v[52:55], v[34:37]
	v_mfma_f32_16x16x32_f16 v[114:117], v[110:113], v[60:63], v[114:117]
	v_cvt_pk_f16_f32 v122, v122, v123
	v_cvt_pk_f16_f32 v123, v124, v125
	ds_write_b64 v88, v[122:123] offset:32
	s_nop 3
	v_cvt_pk_f16_f32 v34, v34, v35
	v_cvt_pk_f16_f32 v35, v36, v37
	ds_write_b64 v90, v[34:35] offset:32
	v_cvt_pk_f16_f32 v114, v114, v115
	v_cvt_pk_f16_f32 v115, v116, v117
	ds_write_b64 v92, v[114:115] offset:32
	s_waitcnt lgkmcnt(0)
	s_barrier
	v_add_u32_e32 v105, s25, v80
	ds_read_b128 v[30:33], v105
	ds_read_b128 v[34:37], v105 offset:64
	ds_read_b128 v[106:109], v105 offset:144
	ds_read_b128 v[110:113], v105 offset:208
	ds_read_b128 v[114:117], v105 offset:288
	ds_read_b128 v[122:125], v105 offset:352
	s_waitcnt lgkmcnt(4)
	v_pk_fma_f16 v118, v30, s36, 0
	v_pk_fma_f16 v119, v31, s37, 0
	v_pk_fma_f16 v120, v32, s38, 0
	v_pk_fma_f16 v121, v33, s39, 0
	v_pk_fma_f16 v26, v34, s72, 0
	v_pk_fma_f16 v27, v35, s73, 0
	v_pk_fma_f16 v28, v36, s74, 0
	v_pk_fma_f16 v29, v37, s75, 0
	ds_read_b128 v[30:33], v105 offset:2592
	ds_read_b128 v[34:37], v105 offset:2656
	s_waitcnt lgkmcnt(4)
	v_pk_fma_f16 v118, v106, s40, v118
	v_pk_fma_f16 v119, v107, s41, v119
	v_pk_fma_f16 v120, v108, s42, v120
	v_pk_fma_f16 v121, v109, s43, v121
	v_pk_fma_f16 v26, v110, s76, v26
	v_pk_fma_f16 v27, v111, s77, v27
	v_pk_fma_f16 v28, v112, s78, v28
	v_pk_fma_f16 v29, v113, s79, v29
	ds_read_b128 v[106:109], v105 offset:2736
	ds_read_b128 v[110:113], v105 offset:2800
	s_waitcnt lgkmcnt(4)
	v_pk_fma_f16 v118, v114, s44, v118
	v_pk_fma_f16 v119, v115, s45, v119
	v_pk_fma_f16 v120, v116, s46, v120
	v_pk_fma_f16 v121, v117, s47, v121
	v_pk_fma_f16 v26, v122, s80, v26
	v_pk_fma_f16 v27, v123, s81, v27
	v_pk_fma_f16 v28, v124, s82, v28
	v_pk_fma_f16 v29, v125, s83, v29
	ds_read_b128 v[114:117], v105 offset:2880
	ds_read_b128 v[122:125], v105 offset:2944
	s_waitcnt lgkmcnt(4)
	v_pk_fma_f16 v118, v30, s48, v118
	v_pk_fma_f16 v119, v31, s49, v119
	v_pk_fma_f16 v120, v32, s50, v120
	v_pk_fma_f16 v121, v33, s51, v121
	v_pk_fma_f16 v26, v34, s84, v26
	v_pk_fma_f16 v27, v35, s85, v27
	v_pk_fma_f16 v28, v36, s86, v28
	v_pk_fma_f16 v29, v37, s87, v29
	ds_read_b128 v[30:33], v105 offset:5184
	ds_read_b128 v[34:37], v105 offset:5248
	s_waitcnt lgkmcnt(4)
	v_pk_fma_f16 v118, v106, s52, v118
	v_pk_fma_f16 v119, v107, s53, v119
	v_pk_fma_f16 v120, v108, s54, v120
	v_pk_fma_f16 v121, v109, s55, v121
	v_pk_fma_f16 v26, v110, s88, v26
	v_pk_fma_f16 v27, v111, s89, v27
	v_pk_fma_f16 v28, v112, s90, v28
	v_pk_fma_f16 v29, v113, s91, v29
	ds_read_b128 v[106:109], v105 offset:5328
	ds_read_b128 v[110:113], v105 offset:5392
	s_waitcnt lgkmcnt(4)
	v_pk_fma_f16 v118, v114, s56, v118
	v_pk_fma_f16 v119, v115, s57, v119
	v_pk_fma_f16 v120, v116, s58, v120
	v_pk_fma_f16 v121, v117, s59, v121
	v_pk_fma_f16 v26, v122, s92, v26
	v_pk_fma_f16 v27, v123, s93, v27
	v_pk_fma_f16 v28, v124, s94, v28
	v_pk_fma_f16 v29, v125, s95, v29
	ds_read_b128 v[114:117], v105 offset:5472
	ds_read_b128 v[122:125], v105 offset:5536
	s_waitcnt lgkmcnt(4)
	v_pk_fma_f16 v118, v30, s60, v118
	v_pk_fma_f16 v119, v31, s61, v119
	v_pk_fma_f16 v120, v32, s62, v120
	v_pk_fma_f16 v121, v33, s63, v121
	v_pk_fma_f16 v26, v34, s96, v26
	v_pk_fma_f16 v27, v35, s97, v27
	v_pk_fma_f16 v28, v36, s98, v28
	v_pk_fma_f16 v29, v37, s99, v29
	s_waitcnt lgkmcnt(2)
	v_pk_fma_f16 v118, v106, s64, v118
	v_pk_fma_f16 v119, v107, s65, v119
	v_pk_fma_f16 v120, v108, s66, v120
	v_pk_fma_f16 v121, v109, s67, v121
	v_pk_fma_f16 v26, v110, s8, v26
	v_pk_fma_f16 v27, v111, s9, v27
	v_pk_fma_f16 v28, v112, s10, v28
	v_pk_fma_f16 v29, v113, s11, v29
	s_waitcnt lgkmcnt(0)
	v_pk_fma_f16 v26, v122, s12, v26
	v_pk_fma_f16 v27, v123, s13, v27
	v_pk_fma_f16 v28, v124, s14, v28
	v_pk_fma_f16 v29, v125, s15, v29
	v_pk_fma_f16 v109, v114, s68, v118
	v_pk_fma_f16 v123, v115, s69, v119
	v_pk_fma_f16 v122, v116, s70, v120
	v_pk_fma_f16 v105, v117, s71, v121
	v_mov_b64_e32 v[114:115], s[22:23]
	v_fma_mix_f32 v106, |v109|, s31, v104 op_sel_hi:[1,0,0]
	v_fma_mix_f32 v107, |v109|, s31, v104 op_sel:[1,0,0] op_sel_hi:[1,0,0]
	v_rcp_f32_e32 v106, v106
	v_rcp_f32_e32 v107, v107
	v_fma_mix_f32 v110, v109, s100, 0 op_sel_hi:[1,0,0]
	v_fma_mix_f32 v111, v109, s100, 0 op_sel:[1,0,0] op_sel_hi:[1,0,0]
	v_mul_f32_e64 v110, v110, -v110
	v_mul_f32_e64 v111, v111, -v111
	v_pk_fma_f32 v[116:117], v[106:107], s[24:25], v[114:115] op_sel_hi:[1,0,0]
	v_exp_f32_e32 v110, v110
	v_pk_fma_f32 v[116:117], v[116:117], v[106:107], s[26:27] op_sel_hi:[1,1,0]
	v_exp_f32_e32 v111, v111
	v_pk_fma_f32 v[116:117], v[116:117], v[106:107], s[28:29] op_sel_hi:[1,1,0]
	v_pk_max_f16 v112, v109, 0
	v_pk_fma_f32 v[116:117], v[116:117], v[106:107], s[30:31] op_sel_hi:[1,1,0]
	v_pk_mul_f32 v[106:107], v[106:107], v[116:117]
	v_pk_mul_f32 v[106:107], v[110:111], v[106:107]
	v_fma_mixlo_f16 v109, -|v109|, v106, v112 op_sel_hi:[1,0,1]
	v_fma_mixhi_f16 v109, -|v109|, v107, v112 op_sel:[1,0,1] op_sel_hi:[1,0,1]
	v_fma_mix_f32 v106, |v123|, s31, v104 op_sel_hi:[1,0,0]
	v_fma_mix_f32 v107, |v123|, s31, v104 op_sel:[1,0,0] op_sel_hi:[1,0,0]
	v_rcp_f32_e32 v106, v106
	v_rcp_f32_e32 v107, v107
	v_fma_mix_f32 v110, v123, s100, 0 op_sel_hi:[1,0,0]
	v_fma_mix_f32 v111, v123, s100, 0 op_sel:[1,0,0] op_sel_hi:[1,0,0]
	v_mul_f32_e64 v110, v110, -v110
	v_mul_f32_e64 v111, v111, -v111
	v_pk_fma_f32 v[116:117], v[106:107], s[24:25], v[114:115] op_sel_hi:[1,0,0]
	v_exp_f32_e32 v110, v110
	v_pk_fma_f32 v[116:117], v[116:117], v[106:107], s[26:27] op_sel_hi:[1,1,0]
	v_exp_f32_e32 v111, v111
	v_pk_fma_f32 v[116:117], v[116:117], v[106:107], s[28:29] op_sel_hi:[1,1,0]
	v_pk_max_f16 v112, v123, 0
	v_pk_fma_f32 v[116:117], v[116:117], v[106:107], s[30:31] op_sel_hi:[1,1,0]
	v_pk_mul_f32 v[106:107], v[106:107], v[116:117]
	v_pk_mul_f32 v[106:107], v[110:111], v[106:107]
	v_fma_mixlo_f16 v123, -|v123|, v106, v112 op_sel_hi:[1,0,1]
	v_fma_mixhi_f16 v123, -|v123|, v107, v112 op_sel:[1,0,1] op_sel_hi:[1,0,1]
	v_fma_mix_f32 v106, |v122|, s31, v104 op_sel_hi:[1,0,0]
	v_fma_mix_f32 v107, |v122|, s31, v104 op_sel:[1,0,0] op_sel_hi:[1,0,0]
	v_rcp_f32_e32 v106, v106
	v_rcp_f32_e32 v107, v107
	v_fma_mix_f32 v110, v122, s100, 0 op_sel_hi:[1,0,0]
	v_fma_mix_f32 v111, v122, s100, 0 op_sel:[1,0,0] op_sel_hi:[1,0,0]
	v_mul_f32_e64 v110, v110, -v110
	v_mul_f32_e64 v111, v111, -v111
	v_pk_fma_f32 v[116:117], v[106:107], s[24:25], v[114:115] op_sel_hi:[1,0,0]
	v_exp_f32_e32 v110, v110
	v_pk_fma_f32 v[116:117], v[116:117], v[106:107], s[26:27] op_sel_hi:[1,1,0]
	v_exp_f32_e32 v111, v111
	v_pk_fma_f32 v[116:117], v[116:117], v[106:107], s[28:29] op_sel_hi:[1,1,0]
	v_pk_max_f16 v112, v122, 0
	v_pk_fma_f32 v[116:117], v[116:117], v[106:107], s[30:31] op_sel_hi:[1,1,0]
	v_pk_mul_f32 v[106:107], v[106:107], v[116:117]
	v_pk_mul_f32 v[106:107], v[110:111], v[106:107]
	v_fma_mixlo_f16 v122, -|v122|, v106, v112 op_sel_hi:[1,0,1]
	v_fma_mixhi_f16 v122, -|v122|, v107, v112 op_sel:[1,0,1] op_sel_hi:[1,0,1]
	v_fma_mix_f32 v106, |v105|, s31, v104 op_sel_hi:[1,0,0]
	v_fma_mix_f32 v107, |v105|, s31, v104 op_sel:[1,0,0] op_sel_hi:[1,0,0]
	v_rcp_f32_e32 v106, v106
	v_rcp_f32_e32 v107, v107
	v_fma_mix_f32 v110, v105, s100, 0 op_sel_hi:[1,0,0]
	v_fma_mix_f32 v111, v105, s100, 0 op_sel:[1,0,0] op_sel_hi:[1,0,0]
	v_mul_f32_e64 v110, v110, -v110
	v_mul_f32_e64 v111, v111, -v111
	v_pk_fma_f32 v[116:117], v[106:107], s[24:25], v[114:115] op_sel_hi:[1,0,0]
	v_exp_f32_e32 v110, v110
	v_pk_fma_f32 v[116:117], v[116:117], v[106:107], s[26:27] op_sel_hi:[1,1,0]
	v_exp_f32_e32 v111, v111
	v_pk_fma_f32 v[116:117], v[116:117], v[106:107], s[28:29] op_sel_hi:[1,1,0]
	v_pk_max_f16 v112, v105, 0
	v_pk_fma_f32 v[116:117], v[116:117], v[106:107], s[30:31] op_sel_hi:[1,1,0]
	v_pk_mul_f32 v[106:107], v[106:107], v[116:117]
	v_pk_mul_f32 v[106:107], v[110:111], v[106:107]
	v_fma_mixlo_f16 v105, -|v105|, v106, v112 op_sel_hi:[1,0,1]
	v_fma_mixhi_f16 v105, -|v105|, v107, v112 op_sel:[1,0,1] op_sel_hi:[1,0,1]
	v_pk_mul_f16 v26, v26, v109
	v_pk_mul_f16 v27, v27, v123
	v_pk_mul_f16 v28, v28, v122
	s_nop 0
	v_pk_mul_f16 v29, v29, v105
	v_add_u32_e32 v30, s25, v78
	ds_write_b128 v30, v[26:29]
	s_waitcnt vmcnt(0)
	ds_write_b128 v39, v[22:25]
	s_and_saveexec_b64 s[32:33], s[4:5]
	s_cbranch_execz .LBB4_36
	ds_write_b128 v39, v[18:21] offset:8192
	s_branch .LBB4_36
